# v7: + P7 mid-segment LDS wait dropped, P7 SP2 stage DMA issues moved into the MFMA blocks (vmcnt 2/5)
# baseline (speedup 1.0000x reference)
.LBB0_782:
	ds_read_b64_tr_b16 v[26:27], v228 offset:0
	ds_read_b64_tr_b16 v[28:29], v228 offset:1024
	ds_read_b64_tr_b16 v[30:31], v228 offset:8192
	ds_read_b64_tr_b16 v[32:33], v228 offset:9216
	ds_read_b64_tr_b16 v[18:19], v232 offset:0
	ds_read_b64_tr_b16 v[20:21], v232 offset:1024
	ds_read_b64_tr_b16 v[22:23], v232 offset:8192
	ds_read_b64_tr_b16 v[24:25], v232 offset:9216
	ds_read_b64_tr_b16 v[10:11], v229 offset:0
	ds_read_b64_tr_b16 v[12:13], v229 offset:1024
	ds_read_b64_tr_b16 v[14:15], v229 offset:8192
	ds_read_b64_tr_b16 v[16:17], v229 offset:9216
	ds_read_b64_tr_b16 v[2:3], v233 offset:0
	ds_read_b64_tr_b16 v[4:5], v233 offset:1024
	ds_read_b64_tr_b16 v[6:7], v233 offset:8192
	ds_read_b64_tr_b16 v[8:9], v233 offset:9216
	v_lshl_add_u64 v[68:69], s[42:43], 0, v[220:221]
	s_add_i32 m0, s15, 0xc000
	s_nop 0
	ds_read_b128 v[58:61], v236
	ds_read_b128 v[62:65], v236 offset:1024
	ds_read_b128 v[50:53], v236 offset:2048
	ds_read_b128 v[54:57], v236 offset:3072
	ds_read_b128 v[42:45], v236 offset:4096
	ds_read_b128 v[46:49], v236 offset:5120
	ds_read_b128 v[34:37], v236 offset:6144
	ds_read_b128 v[38:41], v236 offset:7168
	global_load_lds_dwordx4 v[68:69], off
	v_lshl_add_u64 v[68:69], s[42:43], 0, v[222:223]
	s_add_i32 m0, s15, 0xe000
	s_nop 0
	global_load_lds_dwordx4 v[68:69], off
	s_cmp_eq_u32 s100, 3
	s_cbranch_scc1 .Lp7vg_w11_a1
	s_waitcnt vmcnt(8)
	s_branch .Lp7vg_wd_a1

.Lp7vg_ni_a:
	s_add_u32 s2, s42, 0xfffc0080
	s_addc_u32 s3, s43, -1
	s_cmp_eq_u32 s64, 12
	s_cselect_b32 s5, s23, s3
	s_cselect_b32 s4, s25, s2
	s_cselect_b32 s45, s35, s63
	s_cselect_b32 s44, s61, s62
	s_barrier
	s_setprio 1
	s_waitcnt lgkmcnt(0)
	v_mfma_scale_f32_16x16x128_f8f6f4 v[202:205], v[26:33], v[58:65], v[202:205], v226, v226 op_sel_hi:[0,0,0]
	v_mfma_scale_f32_16x16x128_f8f6f4 v[198:201], v[18:25], v[58:65], v[198:201], v226, v226 op_sel_hi:[0,0,0]
	v_mfma_scale_f32_16x16x128_f8f6f4 v[186:189], v[26:33], v[50:57], v[186:189], v226, v226 op_sel_hi:[0,0,0]
	v_mfma_scale_f32_16x16x128_f8f6f4 v[182:185], v[18:25], v[50:57], v[182:185], v226, v226 op_sel_hi:[0,0,0]
	v_mfma_scale_f32_16x16x128_f8f6f4 v[170:173], v[26:33], v[42:49], v[170:173], v226, v226 op_sel_hi:[0,0,0]
	v_mfma_scale_f32_16x16x128_f8f6f4 v[166:169], v[18:25], v[42:49], v[166:169], v226, v226 op_sel_hi:[0,0,0]
	v_mfma_scale_f32_16x16x128_f8f6f4 v[154:157], v[26:33], v[34:41], v[154:157], v226, v226 op_sel_hi:[0,0,0]
	v_mfma_scale_f32_16x16x128_f8f6f4 v[150:153], v[18:25], v[34:41], v[150:153], v226, v226 op_sel_hi:[0,0,0]
	s_setprio 0
	s_setprio 1
	v_mfma_scale_f32_16x16x128_f8f6f4 v[194:197], v[10:17], v[58:65], v[194:197], v226, v226 op_sel_hi:[0,0,0]
	v_mfma_scale_f32_16x16x128_f8f6f4 v[190:193], v[2:9], v[58:65], v[190:193], v226, v226 op_sel_hi:[0,0,0]
	v_mfma_scale_f32_16x16x128_f8f6f4 v[178:181], v[10:17], v[50:57], v[178:181], v226, v226 op_sel_hi:[0,0,0]
	v_mfma_scale_f32_16x16x128_f8f6f4 v[174:177], v[2:9], v[50:57], v[174:177], v226, v226 op_sel_hi:[0,0,0]
	v_mfma_scale_f32_16x16x128_f8f6f4 v[162:165], v[10:17], v[42:49], v[162:165], v226, v226 op_sel_hi:[0,0,0]
	v_mfma_scale_f32_16x16x128_f8f6f4 v[158:161], v[2:9], v[42:49], v[158:161], v226, v226 op_sel_hi:[0,0,0]
	v_mfma_scale_f32_16x16x128_f8f6f4 v[146:149], v[10:17], v[34:41], v[146:149], v226, v226 op_sel_hi:[0,0,0]
	v_mfma_scale_f32_16x16x128_f8f6f4 v[142:145], v[2:9], v[34:41], v[142:145], v226, v226 op_sel_hi:[0,0,0]
	s_setprio 0
	s_barrier
	s_add_u32 s2, s44, 0x1000
	s_addc_u32 s3, s45, 0
	ds_read_b128 v[58:61], v236 offset:16384
	ds_read_b128 v[62:65], v236 offset:17408
	ds_read_b128 v[50:53], v236 offset:18432
	ds_read_b128 v[54:57], v236 offset:19456
	ds_read_b128 v[42:45], v236 offset:20480
	ds_read_b128 v[46:49], v236 offset:21504
	ds_read_b128 v[34:37], v236 offset:22528
	ds_read_b128 v[38:41], v236 offset:23552
	s_andn2_b64 vcc, exec, s[40:41]
	s_cmp_eq_u32 s100, 3
	s_cbranch_scc1 .Lp7dma_w5_a
	s_waitcnt vmcnt(2)
	s_branch .Lp7dma_wd_a

.Lp7dma_wd_a:
	s_waitcnt lgkmcnt(0)
	s_barrier
	s_cbranch_vccnz .Lp7dma_skip_b
	s_setprio 1
	s_waitcnt lgkmcnt(0)
	v_mfma_scale_f32_16x16x128_f8f6f4 v[138:141], v[26:33], v[58:65], v[138:141], v226, v226 op_sel_hi:[0,0,0]
	v_mfma_scale_f32_16x16x128_f8f6f4 v[134:137], v[18:25], v[58:65], v[134:137], v226, v226 op_sel_hi:[0,0,0]
	s_mov_b32 m0, s19
	v_lshl_add_u64 v[68:69], s[44:45], 0, v[214:215]
	global_load_lds_dwordx4 v[68:69], off
	v_mfma_scale_f32_16x16x128_f8f6f4 v[122:125], v[26:33], v[50:57], v[122:125], v226, v226 op_sel_hi:[0,0,0]
	v_mfma_scale_f32_16x16x128_f8f6f4 v[118:121], v[18:25], v[50:57], v[118:121], v226, v226 op_sel_hi:[0,0,0]
	v_lshl_add_u64 v[68:69], s[44:45], 0, v[218:219]
	s_mov_b32 m0, s33
	s_nop 0
	global_load_lds_dwordx4 v[68:69], off
	v_mfma_scale_f32_16x16x128_f8f6f4 v[106:109], v[26:33], v[42:49], v[106:109], v226, v226 op_sel_hi:[0,0,0]
	v_mfma_scale_f32_16x16x128_f8f6f4 v[102:105], v[18:25], v[42:49], v[102:105], v226, v226 op_sel_hi:[0,0,0]
	v_lshl_add_u64 v[68:69], s[2:3], 0, v[214:215]
	s_mov_b32 m0, s37
	v_lshl_add_u64 v[224:225], s[4:5], 0, v[216:217]
	global_load_lds_dwordx4 v[68:69], off
	v_mfma_scale_f32_16x16x128_f8f6f4 v[90:93], v[26:33], v[34:41], v[90:93], v226, v226 op_sel_hi:[0,0,0]
	v_mfma_scale_f32_16x16x128_f8f6f4 v[86:89], v[18:25], v[34:41], v[86:89], v226, v226 op_sel_hi:[0,0,0]
	s_setprio 0
	s_setprio 1
	v_mfma_scale_f32_16x16x128_f8f6f4 v[130:133], v[10:17], v[58:65], v[130:133], v226, v226 op_sel_hi:[0,0,0]
	v_lshl_add_u64 v[68:69], s[2:3], 0, v[218:219]
	s_mov_b32 m0, s39
	v_cndmask_b32_e64 v66, 0, 1, s[40:41]
	global_load_lds_dwordx4 v[68:69], off
	v_mfma_scale_f32_16x16x128_f8f6f4 v[126:129], v[2:9], v[58:65], v[126:129], v226, v226 op_sel_hi:[0,0,0]
	v_mfma_scale_f32_16x16x128_f8f6f4 v[114:117], v[10:17], v[50:57], v[114:117], v226, v226 op_sel_hi:[0,0,0]
	v_lshl_add_u64 v[68:69], s[4:5], 0, v[212:213]
	s_mov_b32 m0, s15
	v_cmp_ne_u32_e64 s[2:3], 1, v66
	global_load_lds_dwordx4 v[68:69], off
	v_mfma_scale_f32_16x16x128_f8f6f4 v[110:113], v[2:9], v[50:57], v[110:113], v226, v226 op_sel_hi:[0,0,0]
	v_mfma_scale_f32_16x16x128_f8f6f4 v[98:101], v[10:17], v[42:49], v[98:101], v226, v226 op_sel_hi:[0,0,0]
	s_mov_b32 m0, s49
	s_nop 0
	global_load_lds_dwordx4 v[224:225], off
	v_mfma_scale_f32_16x16x128_f8f6f4 v[94:97], v[2:9], v[42:49], v[94:97], v226, v226 op_sel_hi:[0,0,0]
	v_mfma_scale_f32_16x16x128_f8f6f4 v[82:85], v[10:17], v[34:41], v[82:85], v226, v226 op_sel_hi:[0,0,0]
	v_mfma_scale_f32_16x16x128_f8f6f4 v[78:81], v[2:9], v[34:41], v[78:81], v226, v226 op_sel_hi:[0,0,0]
	s_setprio 0
.LBB0_790:
	s_barrier
	ds_read_b64_tr_b16 v[26:27], v230 offset:0
	ds_read_b64_tr_b16 v[28:29], v230 offset:1024
	ds_read_b64_tr_b16 v[30:31], v230 offset:8192
	ds_read_b64_tr_b16 v[32:33], v230 offset:9216
	ds_read_b64_tr_b16 v[18:19], v234 offset:0
	ds_read_b64_tr_b16 v[20:21], v234 offset:1024
	ds_read_b64_tr_b16 v[22:23], v234 offset:8192
	ds_read_b64_tr_b16 v[24:25], v234 offset:9216
	ds_read_b64_tr_b16 v[10:11], v231 offset:0
	ds_read_b64_tr_b16 v[12:13], v231 offset:1024
	ds_read_b64_tr_b16 v[14:15], v231 offset:8192
	ds_read_b64_tr_b16 v[16:17], v231 offset:9216
	ds_read_b64_tr_b16 v[2:3], v235 offset:0
	ds_read_b64_tr_b16 v[4:5], v235 offset:1024
	ds_read_b64_tr_b16 v[6:7], v235 offset:8192
	ds_read_b64_tr_b16 v[8:9], v235 offset:9216
	s_add_u32 s4, s4, 0x40000
	s_addc_u32 s5, s5, 0
	s_mov_b32 m0, s50
	v_lshl_add_u64 v[240:241], s[4:5], 0, v[212:213]
	s_nop 0
	ds_read_b128 v[58:61], v236 offset:32768
	ds_read_b128 v[62:65], v236 offset:33792
	ds_read_b128 v[50:53], v236 offset:34816
	ds_read_b128 v[54:57], v236 offset:35840
	ds_read_b128 v[42:45], v236 offset:36864
	ds_read_b128 v[46:49], v236 offset:37888
	ds_read_b128 v[34:37], v236 offset:38912
	ds_read_b128 v[38:41], v236 offset:39936
	global_load_lds_dwordx4 v[240:241], off
	v_lshl_add_u64 v[240:241], s[4:5], 0, v[216:217]
	s_mov_b32 m0, s51
	s_nop 0
	global_load_lds_dwordx4 v[240:241], off
	s_cmp_eq_u32 s100, 3
	s_cbranch_scc1 .Lp7vg_w11_b1
	s_waitcnt vmcnt(8)
	s_branch .Lp7vg_wd_b1

.Lp7vg_ni_b:
	s_add_u32 s46, s44, 0x84000
	s_addc_u32 s47, s45, 0
	s_barrier
	s_setprio 1
	s_waitcnt lgkmcnt(0)
	v_mfma_scale_f32_16x16x128_f8f6f4 v[202:205], v[26:33], v[58:65], v[202:205], v226, v226 op_sel_hi:[0,0,0]
	v_mfma_scale_f32_16x16x128_f8f6f4 v[198:201], v[18:25], v[58:65], v[198:201], v226, v226 op_sel_hi:[0,0,0]
	v_mfma_scale_f32_16x16x128_f8f6f4 v[186:189], v[26:33], v[50:57], v[186:189], v226, v226 op_sel_hi:[0,0,0]
	v_mfma_scale_f32_16x16x128_f8f6f4 v[182:185], v[18:25], v[50:57], v[182:185], v226, v226 op_sel_hi:[0,0,0]
	v_mfma_scale_f32_16x16x128_f8f6f4 v[170:173], v[26:33], v[42:49], v[170:173], v226, v226 op_sel_hi:[0,0,0]
	v_mfma_scale_f32_16x16x128_f8f6f4 v[166:169], v[18:25], v[42:49], v[166:169], v226, v226 op_sel_hi:[0,0,0]
	v_mfma_scale_f32_16x16x128_f8f6f4 v[154:157], v[26:33], v[34:41], v[154:157], v226, v226 op_sel_hi:[0,0,0]
	v_mfma_scale_f32_16x16x128_f8f6f4 v[150:153], v[18:25], v[34:41], v[150:153], v226, v226 op_sel_hi:[0,0,0]
	s_setprio 0
	s_setprio 1
	v_mfma_scale_f32_16x16x128_f8f6f4 v[194:197], v[10:17], v[58:65], v[194:197], v226, v226 op_sel_hi:[0,0,0]
	v_mfma_scale_f32_16x16x128_f8f6f4 v[190:193], v[2:9], v[58:65], v[190:193], v226, v226 op_sel_hi:[0,0,0]
	v_mfma_scale_f32_16x16x128_f8f6f4 v[178:181], v[10:17], v[50:57], v[178:181], v226, v226 op_sel_hi:[0,0,0]
	v_mfma_scale_f32_16x16x128_f8f6f4 v[174:177], v[2:9], v[50:57], v[174:177], v226, v226 op_sel_hi:[0,0,0]
	v_mfma_scale_f32_16x16x128_f8f6f4 v[162:165], v[10:17], v[42:49], v[162:165], v226, v226 op_sel_hi:[0,0,0]
	v_mfma_scale_f32_16x16x128_f8f6f4 v[158:161], v[2:9], v[42:49], v[158:161], v226, v226 op_sel_hi:[0,0,0]
	v_mfma_scale_f32_16x16x128_f8f6f4 v[146:149], v[10:17], v[34:41], v[146:149], v226, v226 op_sel_hi:[0,0,0]
	v_mfma_scale_f32_16x16x128_f8f6f4 v[142:145], v[2:9], v[34:41], v[142:145], v226, v226 op_sel_hi:[0,0,0]
	s_setprio 0
	s_barrier
	ds_read_b128 v[58:61], v236 offset:49152
	ds_read_b128 v[62:65], v236 offset:50176
	ds_read_b128 v[50:53], v236 offset:51200
	ds_read_b128 v[54:57], v236 offset:52224
	ds_read_b128 v[42:45], v236 offset:53248
	ds_read_b128 v[46:49], v236 offset:54272
	ds_read_b128 v[34:37], v236 offset:55296
	ds_read_b128 v[38:41], v236 offset:56320
	s_and_b64 vcc, exec, s[2:3]
	s_cmp_eq_u32 s100, 3
	s_cbranch_scc1 .Lp7dma_w5_b
	s_waitcnt vmcnt(2)
	s_branch .Lp7dma_wd_b

.Lp7dma_wd_b:
	s_waitcnt lgkmcnt(0)
	s_barrier
	s_cbranch_vccnz .Lp7dma_skip_d
	s_setprio 1
	s_waitcnt lgkmcnt(0)
	v_mfma_scale_f32_16x16x128_f8f6f4 v[138:141], v[26:33], v[58:65], v[138:141], v226, v226 op_sel_hi:[0,0,0]
	v_mfma_scale_f32_16x16x128_f8f6f4 v[134:137], v[18:25], v[58:65], v[134:137], v226, v226 op_sel_hi:[0,0,0]
	v_lshl_add_u64 v[240:241], s[46:47], 0, v[214:215]
	s_add_i32 m0, s15, 0x18000
	s_nop 0
	global_load_lds_dwordx4 v[240:241], off
	v_mfma_scale_f32_16x16x128_f8f6f4 v[122:125], v[26:33], v[50:57], v[122:125], v226, v226 op_sel_hi:[0,0,0]
	v_mfma_scale_f32_16x16x128_f8f6f4 v[118:121], v[18:25], v[50:57], v[118:121], v226, v226 op_sel_hi:[0,0,0]
	s_add_i32 m0, s15, 0x1a000
	v_lshl_add_u64 v[240:241], s[46:47], 0, v[218:219]
	global_load_lds_dwordx4 v[240:241], off
	v_mfma_scale_f32_16x16x128_f8f6f4 v[106:109], v[26:33], v[42:49], v[106:109], v226, v226 op_sel_hi:[0,0,0]
	v_mfma_scale_f32_16x16x128_f8f6f4 v[102:105], v[18:25], v[42:49], v[102:105], v226, v226 op_sel_hi:[0,0,0]
	s_add_u32 s44, s44, 0x85000
	s_addc_u32 s45, s45, 0
	v_lshl_add_u64 v[240:241], s[44:45], 0, v[214:215]
	s_add_i32 m0, s15, 0x1c000
	v_lshl_add_u64 v[68:69], v[68:69], 0, s[10:11]
	global_load_lds_dwordx4 v[240:241], off
	v_mfma_scale_f32_16x16x128_f8f6f4 v[90:93], v[26:33], v[34:41], v[90:93], v226, v226 op_sel_hi:[0,0,0]
	v_mfma_scale_f32_16x16x128_f8f6f4 v[86:89], v[18:25], v[34:41], v[86:89], v226, v226 op_sel_hi:[0,0,0]
	s_setprio 0
	s_setprio 1
	v_mfma_scale_f32_16x16x128_f8f6f4 v[130:133], v[10:17], v[58:65], v[130:133], v226, v226 op_sel_hi:[0,0,0]
	v_lshl_add_u64 v[240:241], s[44:45], 0, v[218:219]
	s_add_i32 m0, s15, 0x1e000
	s_nop 0
	global_load_lds_dwordx4 v[240:241], off
	v_mfma_scale_f32_16x16x128_f8f6f4 v[126:129], v[2:9], v[58:65], v[126:129], v226, v226 op_sel_hi:[0,0,0]
	v_mfma_scale_f32_16x16x128_f8f6f4 v[114:117], v[10:17], v[50:57], v[114:117], v226, v226 op_sel_hi:[0,0,0]
	s_mov_b32 m0, s54
	s_nop 0
	global_load_lds_dwordx4 v[68:69], off
	v_mfma_scale_f32_16x16x128_f8f6f4 v[110:113], v[2:9], v[50:57], v[110:113], v226, v226 op_sel_hi:[0,0,0]
	v_mfma_scale_f32_16x16x128_f8f6f4 v[98:101], v[10:17], v[42:49], v[98:101], v226, v226 op_sel_hi:[0,0,0]
	v_lshl_add_u64 v[68:69], v[224:225], 0, s[10:11]
	s_mov_b32 m0, s55
	s_nop 0
	global_load_lds_dwordx4 v[68:69], off
	v_mfma_scale_f32_16x16x128_f8f6f4 v[94:97], v[2:9], v[42:49], v[94:97], v226, v226 op_sel_hi:[0,0,0]
	v_mfma_scale_f32_16x16x128_f8f6f4 v[82:85], v[10:17], v[34:41], v[82:85], v226, v226 op_sel_hi:[0,0,0]
	v_mfma_scale_f32_16x16x128_f8f6f4 v[78:81], v[2:9], v[34:41], v[78:81], v226, v226 op_sel_hi:[0,0,0]
	s_setprio 0
	s_branch .LBB0_781
.Lp7dma_skip_b:
	s_mov_b32 m0, s19
	v_lshl_add_u64 v[68:69], s[44:45], 0, v[214:215]
	global_load_lds_dwordx4 v[68:69], off
	v_lshl_add_u64 v[68:69], s[44:45], 0, v[218:219]
	s_mov_b32 m0, s33
	s_nop 0
	global_load_lds_dwordx4 v[68:69], off
	v_lshl_add_u64 v[68:69], s[2:3], 0, v[214:215]
	s_mov_b32 m0, s37
	v_lshl_add_u64 v[224:225], s[4:5], 0, v[216:217]
	global_load_lds_dwordx4 v[68:69], off
	v_lshl_add_u64 v[68:69], s[2:3], 0, v[218:219]
	s_mov_b32 m0, s39
	v_cndmask_b32_e64 v66, 0, 1, s[40:41]
	global_load_lds_dwordx4 v[68:69], off
	v_lshl_add_u64 v[68:69], s[4:5], 0, v[212:213]
	s_mov_b32 m0, s15
	v_cmp_ne_u32_e64 s[2:3], 1, v66
	global_load_lds_dwordx4 v[68:69], off
	s_mov_b32 m0, s49
	s_nop 0
	global_load_lds_dwordx4 v[224:225], off
	s_branch .LBB0_790
.Lp7dma_skip_d:
	v_lshl_add_u64 v[240:241], s[46:47], 0, v[214:215]
	s_add_i32 m0, s15, 0x18000
	s_nop 0
	global_load_lds_dwordx4 v[240:241], off
	s_add_i32 m0, s15, 0x1a000
	v_lshl_add_u64 v[240:241], s[46:47], 0, v[218:219]
	global_load_lds_dwordx4 v[240:241], off
	s_add_u32 s44, s44, 0x85000
	s_addc_u32 s45, s45, 0
	v_lshl_add_u64 v[240:241], s[44:45], 0, v[214:215]
	s_add_i32 m0, s15, 0x1c000
	v_lshl_add_u64 v[68:69], v[68:69], 0, s[10:11]
	global_load_lds_dwordx4 v[240:241], off
	v_lshl_add_u64 v[240:241], s[44:45], 0, v[218:219]
	s_add_i32 m0, s15, 0x1e000
	s_nop 0
	global_load_lds_dwordx4 v[240:241], off
	s_mov_b32 m0, s54
	s_nop 0
	global_load_lds_dwordx4 v[68:69], off
	v_lshl_add_u64 v[68:69], v[224:225], 0, s[10:11]
	s_mov_b32 m0, s55
	s_nop 0
	global_load_lds_dwordx4 v[68:69], off
	s_branch .LBB0_781
